# conv1r, conversion quota 3 (before attention) / 1 (after attention)
# baseline (speedup 1.0000x reference)
; __device__ __forceinline__ unsigned xb_ld(unsigned* p)              { return __hip_atomic_load(p, __ATOMIC_RELAXED, __HIP_MEMORY_SCOPE_AGENT); }
; __device__ __forceinline__ unsigned xb_add(unsigned* p, unsigned v) { return __hip_atomic_fetch_add(p, v, __ATOMIC_RELAXED, __HIP_MEMORY_SCOPE_AGENT); }
;     ...
;     unsigned ahead = 0xFFFFFFFFu;
;     if (tl == 0 && max_claims > 0) { if (xb_ld(qw) < (unsigned)target) ahead = xb_add(qw, 32u); }
;     for (int nc = 0; nc < max_claims; ++nc) {
;         if (tl == 0) { st[6] = ahead; if (ahead < (unsigned)target && nc + 1 < max_claims) ahead = (ahead + 32u < (unsigned)target) ? xb_add(qw, 32u) : 0xFFFFFFFFu; }
;         __syncthreads();
.LBB0_803:
	s_and_saveexec_b64 s[0:1], s[2:3]
	s_cbranch_execz .LBB0_811
	v_readlane_b32 s14, v254, 27
	s_cmp_lt_u32 s30, 0
	v_cmp_gt_u32_e32 vcc, s25, v129
	v_mov_b32_e32 v139, s14
	s_cselect_b64 s[14:15], -1, 0
	s_and_b64 s[16:17], vcc, s[14:15]
	ds_write_b32 v139, v129
	s_and_saveexec_b64 s[14:15], s[16:17]
	s_cbranch_execz .LBB0_810
	v_cmp_gt_u32_e32 vcc, s27, v129
	v_mov_b32_e32 v129, -1
	s_and_saveexec_b64 s[16:17], vcc
	s_cbranch_execz .LBB0_809
	s_mov_b64 s[20:21], exec
	v_mbcnt_lo_u32_b32 v129, s20, 0
	v_mbcnt_hi_u32_b32 v129, s21, v129
	v_cmp_eq_u32_e32 vcc, 0, v129
	s_and_saveexec_b64 s[18:19], vcc
	s_cbranch_execz .LBB0_808
	s_bcnt1_i32_b64 s20, s[20:21]
	s_lshl_b32 s20, s20, 5
	v_mov_b32_e32 v139, s20
	global_atomic_add v139, v193, v139, s[4:5] sc0

; __device__ __forceinline__ unsigned xb_add(unsigned* p, unsigned v) { return __hip_atomic_fetch_add(p, v, __ATOMIC_RELAXED, __HIP_MEMORY_SCOPE_AGENT); }
;     __device__ __forceinline__ unsigned char* ws() const { return *(unsigned char* const __attribute__((address_space(4)))*)(p + 232); }
;     ...
;     for (int nc = 0; nc < max_claims; ++nc) {
;         if (tl == 0) { st[6] = ahead; if (ahead < (unsigned)target && nc + 1 < max_claims) ahead = (ahead + 32u < (unsigned)target) ? xb_add(qw, 32u) : 0xFFFFFFFFu; }
;         __syncthreads();
;         const unsigned base = st[6];
;         if (base < (unsigned)Q_TOTAL) {
;             const int q0 = (int)base + wave; const bool v0 = q0 < Q_TOTAL, v1 = q0 + 8 < Q_TOTAL, v2 = q0 + 16 < Q_TOTAL, v3 = q0 + 24 < Q_TOTAL;
;             float ta[64], tb[64]; CvtDesc da, db;
;             if (v0) { da = conv_expert_desc(a, ws, q0); cvt_load(da, ta, lane); }
;             if (v1) { db = conv_expert_desc(a, ws, q0 + 8); cvt_load(db, tb, lane); }
;             if (v0) cvt_finish(da, ta, scr, lane);
;             if (v2) { da = conv_expert_desc(a, ws, q0 + 16); cvt_load(da, ta, lane); }
;             if (v1) cvt_finish(db, tb, scr, lane);
;             if (v3) { db = conv_expert_desc(a, ws, q0 + 24); cvt_load(db, tb, lane); }
;             if (v2) cvt_finish(da, ta, scr, lane);
;             if (v3) cvt_finish(db, tb, scr, lane);
;         }
;         if (base >= (unsigned)target) break;
;         __syncthreads();
.LBB0_884:
	s_cmp_ge_u32 s35, s25
	s_mov_b64 s[0:1], -1
	s_cbranch_scc1 .LBB0_802
	s_add_i32 s30, s30, 1
	s_cmp_eq_u32 s30, 1
	s_cselect_b64 s[0:1], -1, 0
	s_barrier
	s_branch .LBB0_802
